# v82 + combine phases: next token's routing triple prefetched behind the current row loads
# speedup vs baseline: 1.0133x; 1.0056x over previous
.LBB0_970:
	s_or_b64 exec, exec, s[0:1]
	s_waitcnt lgkmcnt(0)
	s_barrier
	s_getreg_b32 s0, hwreg(HW_REG_HW_ID, 0, 6)
	s_lshl_b32 s0, s0, 2
	s_add_i32 s0, s0, 0x27000
	v_mov_b32_e32 v0, s0
	ds_read_b32 v0, v0
	v_mov_b32_e32 v1, 0
	v_mov_b32_e32 v4, 0
	s_waitcnt lgkmcnt(0)
	v_readfirstlane_b32 s0, v0
	v_mbcnt_lo_u32_b32 v0, -1, v1
	v_mbcnt_hi_u32_b32 v0, -1, v0
	v_lshl_or_b32 v2, s0, 6, v0
	s_getreg_b32 s0, hwreg(HW_REG_HW_ID, 0, 6)
	s_lshl_b32 s0, s0, 2
	s_add_i32 s0, s0, 0x27000
	v_mov_b32_e32 v0, s0
	ds_read_b32 v0, v0
	v_mov_b32_e32 v1, 0
	s_waitcnt lgkmcnt(0)
	v_readfirstlane_b32 s0, v0
	v_mbcnt_lo_u32_b32 v0, -1, v1
	v_mbcnt_hi_u32_b32 v0, -1, v0
	v_lshl_or_b32 v3, s0, 6, v0
	s_getreg_b32 s0, hwreg(HW_REG_HW_ID, 0, 6)
	s_lshl_b32 s0, s0, 2
	s_add_i32 s0, s0, 0x27000
	v_mov_b32_e32 v0, s0
	ds_read_b32 v0, v0
	v_mov_b32_e32 v1, 0
	s_waitcnt lgkmcnt(0)
	v_readfirstlane_b32 s0, v0
	v_mbcnt_lo_u32_b32 v0, -1, v4
	v_mbcnt_hi_u32_b32 v0, -1, v0
	v_lshl_or_b32 v0, s0, 6, v0
	s_movk_i32 s0, 0x100
	s_nop 0
	v_cmp_gt_i32_e32 vcc, s0, v0
	v_lshl_add_u32 v4, v0, 2, 0
	v_ashrrev_i32_e32 v0, 6, v3
	v_readlane_b32 s0, v253, 30
	s_waitcnt lgkmcnt(0)
	s_barrier
	v_add_u32_e32 v80, s0, v0
	s_movk_i32 s0, 0x4000
	v_cmp_gt_i32_e32 vcc, s0, v80
	s_and_saveexec_b64 s[2:3], vcc
	s_cbranch_execz .LBB0_1014
	v_readlane_b32 s4, v253, 4
	v_and_b32_e32 v1, 63, v2
	v_readlane_b32 s5, v253, 5
	v_lshlrev_b32_e32 v2, 5, v1
	v_mov_b32_e32 v3, 0
	v_readlane_b32 s18, v253, 18
	v_readlane_b32 s19, v253, 19
	v_readlane_b32 s4, v254, 3
	v_lshl_add_u64 v[84:85], s[64:65], 0, v[2:3]
	v_lshl_add_u64 v[82:83], s[18:19], 0, v[2:3]
	v_lshlrev_b32_e32 v2, 4, v1
	v_readlane_b32 s5, v254, 4
	v_lshlrev_b32_e32 v0, 3, v0
	v_ashrrev_i32_e32 v81, 31, v80
	v_lshl_add_u64 v[86:87], s[4:5], 0, v[2:3]
	s_lshl_b32 s4, s72, 6
	v_cmp_gt_u32_e64 s[0:1], 8, v1
	v_add3_u32 v88, s4, v0, v1
	v_readlane_b32 s4, v253, 2
	v_lshlrev_b64 v[0:1], 11, v[80:81]
	v_readlane_b32 s9, v253, 9
	v_readlane_b32 s5, v253, 3
	v_or_b32_e32 v0, v0, v2
	v_readlane_b32 s6, v253, 6
	v_readlane_b32 s7, v253, 7
	v_readlane_b32 s8, v253, 8
	s_lshl_b32 s9, s4, 6
	v_lshl_add_u64 v[0:1], s[70:71], 0, v[0:1]
	s_mov_b64 s[4:5], 0xd60d500
	s_ashr_i32 s75, s74, 31
	v_lshl_add_u64 v[90:91], v[0:1], 0, s[4:5]
	s_lshl_b64 s[4:5], s[74:75], 11
	s_mov_b64 s[6:7], 0
	s_mov_b32 s8, 0x3fb504f3
	v_mov_b32_e32 v81, 0x3727c5ac
	v_readlane_b32 s10, v253, 10
	v_readlane_b32 s11, v253, 11
	v_readlane_b32 s12, v253, 12
	v_readlane_b32 s13, v253, 13
	v_readlane_b32 s14, v253, 14
	v_readlane_b32 s15, v253, 15
	v_readlane_b32 s16, v253, 16
	v_readlane_b32 s17, v253, 17
	v_min_u32_e32 v240, 0x1ffff, v88
	v_mov_b32_e32 v241, 0
	v_readlane_b32 s98, v253, 55
	v_readlane_b32 s99, v253, 56
	v_lshlrev_b64 v[240:241], 2, v[240:241]
	s_nop 1
	v_lshl_add_u64 v[242:243], s[98:99], 0, v[240:241]
	global_load_dword v244, v[242:243], off
	v_readlane_b32 s98, v253, 59
	v_readlane_b32 s99, v253, 60
	s_nop 1
	v_lshl_add_u64 v[242:243], s[98:99], 0, v[240:241]
	global_load_dword v245, v[242:243], off
	v_readlane_b32 s98, v253, 57
	v_readlane_b32 s99, v253, 58
	s_nop 1
	v_lshl_add_u64 v[242:243], s[98:99], 0, v[240:241]
	global_load_dword v246, v[242:243], off
	global_load_dwordx4 v[200:203], v[82:83], off
	global_load_dwordx4 v[204:207], v[82:83], off offset:16
	global_load_dwordx4 v[208:211], v[84:85], off
	global_load_dwordx4 v[212:215], v[84:85], off offset:16
	global_load_dwordx4 v[216:219], v[82:83], off offset:2048
	global_load_dwordx4 v[220:223], v[82:83], off offset:2064
	global_load_dwordx4 v[224:227], v[84:85], off offset:2048
	global_load_dwordx4 v[228:231], v[84:85], off offset:2064
	s_waitcnt vmcnt(0)
	s_branch .LBB0_1012
.LBB0_1011:
	s_or_b64 exec, exec, s[10:11]
	v_add_u32_e32 v0, 0x20000, v80
	v_ashrrev_i32_e32 v1, 31, v0
	v_readlane_b32 s10, v25, 0
	v_lshlrev_b64 v[0:1], 11, v[0:1]
	s_ashr_i32 s11, s10, 31
	global_load_dwordx4 v[52:55], v[90:91], off
	v_lshl_add_u64 v[0:1], v[86:87], 0, v[0:1]
	s_lshl_b64 s[10:11], s[10:11], 11
	global_load_dwordx4 v[48:51], v[0:1], off
	global_load_dwordx4 v[12:15], v[90:91], off offset:1024
	global_load_dwordx4 v[8:11], v[0:1], off offset:1024
	v_lshl_add_u64 v[0:1], v[86:87], 0, s[10:11]
	v_readlane_b32 s12, v25, 1
	global_load_dwordx4 v[56:59], v[0:1], off
	global_load_dwordx4 v[20:23], v[0:1], off offset:1024
	s_ashr_i32 s13, s12, 31
	v_readlane_b32 s14, v25, 2
	s_lshl_b64 s[12:13], s[12:13], 11
	s_ashr_i32 s15, s14, 31
	v_readlane_b32 s16, v25, 3
	v_lshl_add_u64 v[0:1], v[86:87], 0, s[12:13]
	s_lshl_b64 s[14:15], s[14:15], 11
	s_ashr_i32 s17, s16, 31
	v_readlane_b32 s18, v25, 4
	global_load_dwordx4 v[60:63], v[0:1], off
	global_load_dwordx4 v[28:31], v[0:1], off offset:1024
	v_lshl_add_u64 v[0:1], v[86:87], 0, s[14:15]
	s_lshl_b64 s[16:17], s[16:17], 11
	s_ashr_i32 s19, s18, 31
	global_load_dwordx4 v[68:71], v[0:1], off
	global_load_dwordx4 v[36:39], v[0:1], off offset:1024
	v_lshl_add_u64 v[0:1], v[86:87], 0, s[16:17]
	s_lshl_b64 s[18:19], s[18:19], 11
	global_load_dwordx4 v[72:75], v[0:1], off
	global_load_dwordx4 v[40:43], v[0:1], off offset:1024
	v_lshl_add_u64 v[0:1], v[86:87], 0, s[18:19]
	global_load_dwordx4 v[76:79], v[0:1], off
	global_load_dwordx4 v[44:47], v[0:1], off offset:1024
	v_readlane_b32 s20, v25, 5
	s_ashr_i32 s21, s20, 31
	v_readlane_b32 s22, v25, 6
	s_lshl_b64 s[20:21], s[20:21], 11
	s_ashr_i32 s23, s22, 31
	v_readlane_b32 s26, v25, 7
	v_lshl_add_u64 v[0:1], v[86:87], 0, s[20:21]
	s_lshl_b64 s[22:23], s[22:23], 11
	s_ashr_i32 s27, s26, 31
	global_load_dwordx4 v[16:19], v[0:1], off
	s_nop 0
	global_load_dwordx4 v[0:3], v[0:1], off offset:1024
	v_lshl_add_u64 v[4:5], v[86:87], 0, s[22:23]
	s_lshl_b64 s[26:27], s[26:27], 11
	v_readlane_b32 s24, v24, 0
	v_readlane_b32 s10, v24, 1
	v_readlane_b32 s12, v24, 2
	v_readlane_b32 s14, v24, 3
	v_readlane_b32 s16, v24, 4
	v_readlane_b32 s18, v24, 5
	v_readlane_b32 s20, v24, 6
	global_load_dwordx4 v[32:35], v[4:5], off
	s_nop 0
	global_load_dwordx4 v[4:7], v[4:5], off offset:1024
	v_readlane_b32 s22, v24, 7
	v_lshl_add_u64 v[24:25], v[86:87], 0, s[26:27]
	global_load_dwordx4 v[64:67], v[24:25], off
	s_nop 0
	global_load_dwordx4 v[24:27], v[24:25], off offset:1024
	v_add_u32_e32 v80, s74, v80
	v_add_u32_e32 v88, s9, v88
	v_min_u32_e32 v240, 0x1ffff, v88
	v_mov_b32_e32 v241, 0
	v_readlane_b32 s98, v253, 55
	v_readlane_b32 s99, v253, 56
	v_lshlrev_b64 v[240:241], 2, v[240:241]
	s_nop 1
	v_lshl_add_u64 v[242:243], s[98:99], 0, v[240:241]
	global_load_dword v244, v[242:243], off
	v_readlane_b32 s98, v253, 59
	v_readlane_b32 s99, v253, 60
	s_nop 1
	v_lshl_add_u64 v[242:243], s[98:99], 0, v[240:241]
	global_load_dword v245, v[242:243], off
	v_readlane_b32 s98, v253, 57
	v_readlane_b32 s99, v253, 58
	s_nop 1
	v_lshl_add_u64 v[242:243], s[98:99], 0, v[240:241]
	global_load_dword v246, v[242:243], off
	s_waitcnt vmcnt(22)
	v_lshlrev_b32_e32 v92, 16, v52
	v_and_b32_e32 v93, 0xffff0000, v52
	s_waitcnt vmcnt(21)
	v_lshlrev_b32_e32 v94, 16, v48
	v_and_b32_e32 v95, 0xffff0000, v48
	v_lshlrev_b32_e32 v52, 16, v53
	v_and_b32_e32 v53, 0xffff0000, v53
	v_lshlrev_b32_e32 v48, 16, v49
	v_and_b32_e32 v49, 0xffff0000, v49
	v_pk_fma_f32 v[48:49], v[52:53], s[8:9], v[48:49] op_sel_hi:[1,0,1]
	s_waitcnt vmcnt(18)
	v_lshlrev_b32_e32 v52, 16, v57
	v_and_b32_e32 v53, 0xffff0000, v57
	v_pk_fma_f32 v[102:103], s[24:25], v[52:53], v[48:49] op_sel_hi:[0,1,1]
	v_lshlrev_b32_e32 v48, 16, v54
	v_and_b32_e32 v49, 0xffff0000, v54
	v_lshlrev_b32_e32 v52, 16, v50
	v_and_b32_e32 v53, 0xffff0000, v50
	v_pk_fma_f32 v[48:49], v[48:49], s[8:9], v[52:53] op_sel_hi:[1,0,1]
	v_lshlrev_b32_e32 v52, 16, v58
	v_and_b32_e32 v53, 0xffff0000, v58
	v_pk_fma_f32 v[104:105], s[24:25], v[52:53], v[48:49] op_sel_hi:[0,1,1]
	v_lshlrev_b32_e32 v48, 16, v55
	v_and_b32_e32 v49, 0xffff0000, v55
	v_lshlrev_b32_e32 v50, 16, v51
	v_and_b32_e32 v51, 0xffff0000, v51
	v_pk_fma_f32 v[48:49], v[48:49], s[8:9], v[50:51] op_sel_hi:[1,0,1]
	v_lshlrev_b32_e32 v50, 16, v59
	v_and_b32_e32 v51, 0xffff0000, v59
	v_pk_fma_f32 v[58:59], s[24:25], v[50:51], v[48:49] op_sel_hi:[0,1,1]
	v_lshlrev_b32_e32 v48, 16, v12
	v_and_b32_e32 v49, 0xffff0000, v12
	v_lshlrev_b32_e32 v50, 16, v8
	v_and_b32_e32 v51, 0xffff0000, v8
	v_lshlrev_b32_e32 v12, 16, v13
	v_and_b32_e32 v13, 0xffff0000, v13
	v_lshlrev_b32_e32 v8, 16, v9
	v_and_b32_e32 v9, 0xffff0000, v9
	v_pk_fma_f32 v[48:49], v[48:49], s[8:9], v[50:51] op_sel_hi:[1,0,1]
	s_waitcnt vmcnt(17)
	v_lshlrev_b32_e32 v50, 16, v20
	v_and_b32_e32 v51, 0xffff0000, v20
	v_pk_fma_f32 v[8:9], v[12:13], s[8:9], v[8:9] op_sel_hi:[1,0,1]
	v_lshlrev_b32_e32 v12, 16, v21
	v_and_b32_e32 v13, 0xffff0000, v21
	v_pk_fma_f32 v[92:93], v[92:93], s[8:9], v[94:95] op_sel_hi:[1,0,1]
	v_lshlrev_b32_e32 v94, 16, v56
	v_and_b32_e32 v95, 0xffff0000, v56
	v_pk_fma_f32 v[48:49], s[24:25], v[50:51], v[48:49] op_sel_hi:[0,1,1]
	s_waitcnt vmcnt(15)
	v_lshlrev_b32_e32 v54, 16, v28
	v_and_b32_e32 v55, 0xffff0000, v28
	s_waitcnt vmcnt(13)
	v_lshlrev_b32_e32 v56, 16, v36
	v_and_b32_e32 v57, 0xffff0000, v36
	s_waitcnt vmcnt(11)
	v_lshlrev_b32_e32 v52, 16, v40
	v_and_b32_e32 v53, 0xffff0000, v40
	s_waitcnt vmcnt(9)
	v_lshlrev_b32_e32 v50, 16, v44
	v_and_b32_e32 v51, 0xffff0000, v44
	v_pk_fma_f32 v[8:9], s[24:25], v[12:13], v[8:9] op_sel_hi:[0,1,1]
	v_lshlrev_b32_e32 v12, 16, v29
	v_and_b32_e32 v13, 0xffff0000, v29
	v_lshlrev_b32_e32 v20, 16, v37
	v_and_b32_e32 v21, 0xffff0000, v37
	v_lshlrev_b32_e32 v28, 16, v41
	v_and_b32_e32 v29, 0xffff0000, v41
	v_lshlrev_b32_e32 v36, 16, v45
	v_and_b32_e32 v37, 0xffff0000, v45
	v_lshlrev_b32_e32 v40, 16, v14
	v_and_b32_e32 v41, 0xffff0000, v14
	v_lshlrev_b32_e32 v44, 16, v10
	v_and_b32_e32 v45, 0xffff0000, v10
	v_lshlrev_b32_e32 v14, 16, v15
	v_and_b32_e32 v15, 0xffff0000, v15
	v_lshlrev_b32_e32 v10, 16, v11
	v_and_b32_e32 v11, 0xffff0000, v11
	v_lshlrev_b32_e32 v106, 16, v62
	v_and_b32_e32 v107, 0xffff0000, v62
	v_lshlrev_b32_e32 v62, 16, v63
	v_and_b32_e32 v63, 0xffff0000, v63
	v_pk_fma_f32 v[40:41], v[40:41], s[8:9], v[44:45] op_sel_hi:[1,0,1]
	v_lshlrev_b32_e32 v44, 16, v22
	v_and_b32_e32 v45, 0xffff0000, v22
	v_pk_fma_f32 v[10:11], v[14:15], s[8:9], v[10:11] op_sel_hi:[1,0,1]
	v_lshlrev_b32_e32 v14, 16, v23
	v_and_b32_e32 v15, 0xffff0000, v23
	v_lshlrev_b32_e32 v108, 16, v70
	v_and_b32_e32 v109, 0xffff0000, v70
	v_lshlrev_b32_e32 v70, 16, v71
	v_and_b32_e32 v71, 0xffff0000, v71
	v_pk_fma_f32 v[40:41], s[24:25], v[44:45], v[40:41] op_sel_hi:[0,1,1]
	v_lshlrev_b32_e32 v44, 16, v30
	v_and_b32_e32 v45, 0xffff0000, v30
	v_lshlrev_b32_e32 v116, 16, v42
	v_and_b32_e32 v117, 0xffff0000, v42
	v_pk_fma_f32 v[10:11], s[24:25], v[14:15], v[10:11] op_sel_hi:[0,1,1]
	v_lshlrev_b32_e32 v14, 16, v31
	v_and_b32_e32 v15, 0xffff0000, v31
	v_lshlrev_b32_e32 v30, 16, v43
	v_and_b32_e32 v31, 0xffff0000, v43
	v_pk_fma_f32 v[42:43], s[10:11], v[62:63], v[58:59] op_sel_hi:[0,1,1]
	v_lshlrev_b32_e32 v110, 16, v74
	v_and_b32_e32 v111, 0xffff0000, v74
	v_lshlrev_b32_e32 v74, 16, v75
	v_and_b32_e32 v75, 0xffff0000, v75
	v_pk_fma_f32 v[42:43], s[12:13], v[70:71], v[42:43] op_sel_hi:[0,1,1]
	v_lshlrev_b32_e32 v112, 16, v78
	v_and_b32_e32 v113, 0xffff0000, v78
	v_lshlrev_b32_e32 v78, 16, v79
	v_and_b32_e32 v79, 0xffff0000, v79
	v_pk_fma_f32 v[42:43], s[14:15], v[74:75], v[42:43] op_sel_hi:[0,1,1]
	v_lshlrev_b32_e32 v114, 16, v38
	v_and_b32_e32 v115, 0xffff0000, v38
	v_lshlrev_b32_e32 v118, 16, v46
	v_and_b32_e32 v119, 0xffff0000, v46
	v_lshlrev_b32_e32 v22, 16, v39
	v_and_b32_e32 v23, 0xffff0000, v39
	v_lshlrev_b32_e32 v38, 16, v47
	v_and_b32_e32 v39, 0xffff0000, v47
	v_pk_fma_f32 v[42:43], s[16:17], v[78:79], v[42:43] op_sel_hi:[0,1,1]
	s_waitcnt vmcnt(8)
	v_lshlrev_b32_e32 v46, 16, v19
	v_and_b32_e32 v47, 0xffff0000, v19
	v_pk_fma_f32 v[42:43], s[18:19], v[46:47], v[42:43] op_sel_hi:[0,1,1]
	s_waitcnt vmcnt(6)
	v_lshlrev_b32_e32 v46, 16, v35
	v_and_b32_e32 v47, 0xffff0000, v35
	v_pk_fma_f32 v[42:43], s[20:21], v[46:47], v[42:43] op_sel_hi:[0,1,1]
	s_waitcnt vmcnt(4)
	v_lshlrev_b32_e32 v46, 16, v67
	v_and_b32_e32 v47, 0xffff0000, v67
	v_pk_fma_f32 v[42:43], s[22:23], v[46:47], v[42:43] op_sel_hi:[0,1,1]
	v_pk_fma_f32 v[46:47], s[10:11], v[106:107], v[104:105] op_sel_hi:[0,1,1]
	v_pk_fma_f32 v[46:47], s[12:13], v[108:109], v[46:47] op_sel_hi:[0,1,1]
	v_pk_fma_f32 v[46:47], s[14:15], v[110:111], v[46:47] op_sel_hi:[0,1,1]
	v_pk_fma_f32 v[10:11], s[10:11], v[14:15], v[10:11] op_sel_hi:[0,1,1]
	v_pk_fma_f32 v[46:47], s[16:17], v[112:113], v[46:47] op_sel_hi:[0,1,1]
	v_lshlrev_b32_e32 v58, 16, v18
	v_and_b32_e32 v59, 0xffff0000, v18
	v_pk_fma_f32 v[10:11], s[12:13], v[22:23], v[10:11] op_sel_hi:[0,1,1]
	v_pk_fma_f32 v[18:19], s[18:19], v[58:59], v[46:47] op_sel_hi:[0,1,1]
	v_lshlrev_b32_e32 v46, 16, v34
	v_and_b32_e32 v47, 0xffff0000, v34
	v_pk_fma_f32 v[10:11], s[14:15], v[30:31], v[10:11] op_sel_hi:[0,1,1]
	v_lshlrev_b32_e32 v100, 16, v60
	v_and_b32_e32 v101, 0xffff0000, v60
	v_lshlrev_b32_e32 v60, 16, v61
	v_and_b32_e32 v61, 0xffff0000, v61
	v_pk_fma_f32 v[18:19], s[20:21], v[46:47], v[18:19] op_sel_hi:[0,1,1]
	v_lshlrev_b32_e32 v34, 16, v66
	v_and_b32_e32 v35, 0xffff0000, v66
	v_pk_fma_f32 v[10:11], s[16:17], v[38:39], v[10:11] op_sel_hi:[0,1,1]
	v_lshlrev_b32_e32 v14, 16, v3
	v_and_b32_e32 v15, 0xffff0000, v3
	v_lshlrev_b32_e32 v98, 16, v68
	v_and_b32_e32 v99, 0xffff0000, v68
	v_lshlrev_b32_e32 v68, 16, v69
	v_and_b32_e32 v69, 0xffff0000, v69
	v_pk_fma_f32 v[18:19], s[22:23], v[34:35], v[18:19] op_sel_hi:[0,1,1]
	v_pk_fma_f32 v[34:35], s[10:11], v[60:61], v[102:103] op_sel_hi:[0,1,1]
	v_pk_fma_f32 v[10:11], s[18:19], v[14:15], v[10:11] op_sel_hi:[0,1,1]
	v_lshlrev_b32_e32 v14, 16, v7
	v_and_b32_e32 v15, 0xffff0000, v7
	v_pk_fma_f32 v[96:97], s[24:25], v[94:95], v[92:93] op_sel_hi:[0,1,1]
	v_lshlrev_b32_e32 v94, 16, v72
	v_and_b32_e32 v95, 0xffff0000, v72
	v_lshlrev_b32_e32 v72, 16, v73
	v_and_b32_e32 v73, 0xffff0000, v73
	v_pk_fma_f32 v[34:35], s[12:13], v[68:69], v[34:35] op_sel_hi:[0,1,1]
	v_pk_fma_f32 v[10:11], s[20:21], v[14:15], v[10:11] op_sel_hi:[0,1,1]
	s_waitcnt vmcnt(3)
	v_lshlrev_b32_e32 v14, 16, v27
	v_and_b32_e32 v15, 0xffff0000, v27
	v_lshlrev_b32_e32 v92, 16, v76
	v_and_b32_e32 v93, 0xffff0000, v76
	v_lshlrev_b32_e32 v76, 16, v77
	v_and_b32_e32 v77, 0xffff0000, v77
	v_pk_fma_f32 v[34:35], s[14:15], v[72:73], v[34:35] op_sel_hi:[0,1,1]
	v_pk_fma_f32 v[10:11], s[22:23], v[14:15], v[10:11] op_sel_hi:[0,1,1]
	v_pk_fma_f32 v[14:15], s[10:11], v[44:45], v[40:41] op_sel_hi:[0,1,1]
	v_pk_fma_f32 v[34:35], s[16:17], v[76:77], v[34:35] op_sel_hi:[0,1,1]
	v_lshlrev_b32_e32 v46, 16, v17
	v_and_b32_e32 v47, 0xffff0000, v17
	v_pk_fma_f32 v[14:15], s[12:13], v[114:115], v[14:15] op_sel_hi:[0,1,1]
	v_pk_fma_f32 v[34:35], s[18:19], v[46:47], v[34:35] op_sel_hi:[0,1,1]
	v_lshlrev_b32_e32 v46, 16, v33
	v_and_b32_e32 v47, 0xffff0000, v33
	v_pk_fma_f32 v[14:15], s[14:15], v[116:117], v[14:15] op_sel_hi:[0,1,1]
	v_pk_fma_f32 v[34:35], s[20:21], v[46:47], v[34:35] op_sel_hi:[0,1,1]
	v_lshlrev_b32_e32 v46, 16, v65
	v_and_b32_e32 v47, 0xffff0000, v65
	v_pk_fma_f32 v[14:15], s[16:17], v[118:119], v[14:15] op_sel_hi:[0,1,1]
	v_lshlrev_b32_e32 v22, 16, v2
	v_and_b32_e32 v23, 0xffff0000, v2
	v_pk_fma_f32 v[34:35], s[22:23], v[46:47], v[34:35] op_sel_hi:[0,1,1]
	v_pk_fma_f32 v[46:47], s[10:11], v[100:101], v[96:97] op_sel_hi:[0,1,1]
	v_pk_fma_f32 v[2:3], s[18:19], v[22:23], v[14:15] op_sel_hi:[0,1,1]
	v_lshlrev_b32_e32 v14, 16, v6
	v_and_b32_e32 v15, 0xffff0000, v6
	v_pk_fma_f32 v[46:47], s[12:13], v[98:99], v[46:47] op_sel_hi:[0,1,1]
	v_pk_fma_f32 v[2:3], s[20:21], v[14:15], v[2:3] op_sel_hi:[0,1,1]
	v_lshlrev_b32_e32 v6, 16, v26
	v_and_b32_e32 v7, 0xffff0000, v26
	v_pk_fma_f32 v[46:47], s[14:15], v[94:95], v[46:47] op_sel_hi:[0,1,1]
	v_pk_fma_f32 v[2:3], s[22:23], v[6:7], v[2:3] op_sel_hi:[0,1,1]
	v_pk_fma_f32 v[6:7], s[10:11], v[12:13], v[8:9] op_sel_hi:[0,1,1]
	v_pk_fma_f32 v[46:47], s[16:17], v[92:93], v[46:47] op_sel_hi:[0,1,1]
	v_lshlrev_b32_e32 v58, 16, v16
	v_and_b32_e32 v59, 0xffff0000, v16
	v_pk_fma_f32 v[6:7], s[12:13], v[20:21], v[6:7] op_sel_hi:[0,1,1]
	v_pk_fma_f32 v[16:17], s[18:19], v[58:59], v[46:47] op_sel_hi:[0,1,1]
	v_lshlrev_b32_e32 v46, 16, v32
	v_and_b32_e32 v47, 0xffff0000, v32
	v_pk_fma_f32 v[6:7], s[14:15], v[28:29], v[6:7] op_sel_hi:[0,1,1]
	v_pk_fma_f32 v[16:17], s[20:21], v[46:47], v[16:17] op_sel_hi:[0,1,1]
	v_lshlrev_b32_e32 v32, 16, v64
	v_and_b32_e32 v33, 0xffff0000, v64
	v_pk_fma_f32 v[6:7], s[16:17], v[36:37], v[6:7] op_sel_hi:[0,1,1]
	v_lshlrev_b32_e32 v8, 16, v1
	v_and_b32_e32 v9, 0xffff0000, v1
	v_pk_fma_f32 v[16:17], s[22:23], v[32:33], v[16:17] op_sel_hi:[0,1,1]
	v_pk_fma_f32 v[6:7], s[18:19], v[8:9], v[6:7] op_sel_hi:[0,1,1]
	v_lshlrev_b32_e32 v8, 16, v5
	v_and_b32_e32 v9, 0xffff0000, v5
	v_add_f32_e32 v32, 0, v16
	v_pk_fma_f32 v[6:7], s[20:21], v[8:9], v[6:7] op_sel_hi:[0,1,1]
	v_lshlrev_b32_e32 v8, 16, v25
	v_and_b32_e32 v9, 0xffff0000, v25
	v_add_f32_e32 v32, v17, v32
	v_pk_fma_f32 v[6:7], s[22:23], v[8:9], v[6:7] op_sel_hi:[0,1,1]
	v_pk_fma_f32 v[8:9], s[10:11], v[54:55], v[48:49] op_sel_hi:[0,1,1]
	v_add_f32_e32 v32, v34, v32
	v_pk_fma_f32 v[8:9], s[12:13], v[56:57], v[8:9] op_sel_hi:[0,1,1]
	v_add_f32_e32 v32, v35, v32
	v_pk_fma_f32 v[8:9], s[14:15], v[52:53], v[8:9] op_sel_hi:[0,1,1]
	v_add_f32_e32 v32, v18, v32
	v_pk_fma_f32 v[8:9], s[16:17], v[50:51], v[8:9] op_sel_hi:[0,1,1]
	v_lshlrev_b32_e32 v12, 16, v0
	v_and_b32_e32 v13, 0xffff0000, v0
	v_add_f32_e32 v32, v19, v32
	v_pk_fma_f32 v[0:1], s[18:19], v[12:13], v[8:9] op_sel_hi:[0,1,1]
	v_lshlrev_b32_e32 v8, 16, v4
	v_and_b32_e32 v9, 0xffff0000, v4
	v_add_f32_e32 v32, v42, v32
	v_pk_fma_f32 v[0:1], s[20:21], v[8:9], v[0:1] op_sel_hi:[0,1,1]
	v_lshlrev_b32_e32 v4, 16, v24
	v_and_b32_e32 v5, 0xffff0000, v24
	v_add_f32_e32 v32, v43, v32
	v_pk_fma_f32 v[0:1], s[22:23], v[4:5], v[0:1] op_sel_hi:[0,1,1]
	v_add_f32_e32 v4, v0, v32
	v_add_f32_e32 v4, v1, v4
	v_add_f32_e32 v4, v6, v4
	v_add_f32_e32 v4, v7, v4
	v_add_f32_e32 v4, v2, v4
	v_add_f32_e32 v4, v3, v4
	v_add_f32_e32 v4, v10, v4
	v_add_f32_e32 v4, v11, v4
	s_mov_b32 s10, 0x800000
	s_nop 0
	v_add_f32_dpp v4, v4, v4 quad_perm:[1,0,3,2] row_mask:0xf bank_mask:0xf bound_ctrl:1
	s_nop 1
	v_add_f32_dpp v4, v4, v4 quad_perm:[2,3,0,1] row_mask:0xf bank_mask:0xf bound_ctrl:1
	s_nop 1
	v_add_f32_dpp v4, v4, v4 row_half_mirror row_mask:0xf bank_mask:0xf bound_ctrl:1
	s_nop 1
	v_add_f32_dpp v4, v4, v4 row_mirror row_mask:0xf bank_mask:0xf bound_ctrl:1
	v_mov_b32_e32 v5, v4
	s_nop 1
	v_permlane16_swap_b32 v5, v4
	s_nop 0
	v_add_f32_e32 v4, v5, v4
	v_mov_b32_e32 v5, v4
	s_nop 1
	v_permlane32_swap_b32 v4, v5
	s_nop 0
	v_add_f32_e32 v4, v4, v5
	v_mul_f32_e32 v4, 0x3a800000, v4
	v_pk_add_f32 v[26:27], v[16:17], v[4:5] op_sel_hi:[1,0] neg_lo:[0,1] neg_hi:[0,1]
	v_pk_add_f32 v[28:29], v[34:35], v[4:5] op_sel_hi:[1,0] neg_lo:[0,1] neg_hi:[0,1]
	v_pk_mul_f32 v[8:9], v[26:27], v[26:27]
	v_pk_mul_f32 v[12:13], v[28:29], v[28:29]
	v_add_f32_e32 v8, v8, v9
	v_pk_add_f32 v[30:31], v[18:19], v[4:5] op_sel_hi:[1,0] neg_lo:[0,1] neg_hi:[0,1]
	v_add_f32_e32 v8, v12, v8
	v_pk_mul_f32 v[14:15], v[30:31], v[30:31]
	v_add_f32_e32 v8, v13, v8
	v_pk_add_f32 v[32:33], v[42:43], v[4:5] op_sel_hi:[1,0] neg_lo:[0,1] neg_hi:[0,1]
	v_add_f32_e32 v8, v14, v8
	v_pk_mul_f32 v[24:25], v[32:33], v[32:33]
	v_add_f32_e32 v8, v15, v8
	v_pk_add_f32 v[16:17], v[0:1], v[4:5] op_sel_hi:[1,0] neg_lo:[0,1] neg_hi:[0,1]
	v_add_f32_e32 v8, v24, v8
	v_pk_mul_f32 v[0:1], v[16:17], v[16:17]
	v_add_f32_e32 v8, v25, v8
	v_pk_add_f32 v[18:19], v[6:7], v[4:5] op_sel_hi:[1,0] neg_lo:[0,1] neg_hi:[0,1]
	v_add_f32_e32 v0, v0, v8
	v_pk_mul_f32 v[6:7], v[18:19], v[18:19]
	v_add_f32_e32 v0, v1, v0
	v_pk_add_f32 v[20:21], v[2:3], v[4:5] op_sel_hi:[1,0] neg_lo:[0,1] neg_hi:[0,1]
	v_add_f32_e32 v0, v6, v0
	v_pk_mul_f32 v[2:3], v[20:21], v[20:21]
	v_add_f32_e32 v0, v7, v0
	v_pk_add_f32 v[22:23], v[10:11], v[4:5] op_sel_hi:[1,0] neg_lo:[0,1] neg_hi:[0,1]
	v_add_f32_e32 v0, v2, v0
	v_pk_mul_f32 v[4:5], v[22:23], v[22:23]
	v_add_f32_e32 v0, v3, v0
	v_add_f32_e32 v0, v4, v0
	v_add_f32_e32 v0, v5, v0
	s_nop 1
	v_add_f32_dpp v0, v0, v0 quad_perm:[1,0,3,2] row_mask:0xf bank_mask:0xf bound_ctrl:1
	s_nop 1
	v_add_f32_dpp v0, v0, v0 quad_perm:[2,3,0,1] row_mask:0xf bank_mask:0xf bound_ctrl:1
	s_nop 1
	v_add_f32_dpp v0, v0, v0 row_half_mirror row_mask:0xf bank_mask:0xf bound_ctrl:1
	s_nop 1
	v_add_f32_dpp v0, v0, v0 row_mirror row_mask:0xf bank_mask:0xf bound_ctrl:1
	v_mov_b32_e32 v1, v0
	s_nop 1
	v_permlane16_swap_b32 v1, v0
	s_nop 0
	v_add_f32_e32 v0, v1, v0
	v_mov_b32_e32 v1, v0
	s_nop 1
	v_permlane32_swap_b32 v1, v0
	s_nop 0
	v_add_f32_e32 v0, v1, v0
	v_fmamk_f32 v0, v0, 0x3a800000, v81
	v_cmp_gt_f32_e32 vcc, s10, v0
	v_mul_f32_e32 v1, 0x4b800000, v0
	s_mov_b32 s10, 0xf2b00000
	v_cndmask_b32_e32 v0, v0, v1, vcc
	v_rsq_f32_e32 v0, v0
	s_nop 0
	v_mul_f32_e32 v1, 0x45800000, v0
	v_cndmask_b32_e32 v24, v0, v1, vcc
	v_pk_mul_f32 v[26:27], v[26:27], v[24:25] op_sel_hi:[1,0]
	v_pk_mul_f32 v[16:17], v[16:17], v[24:25] op_sel_hi:[1,0]
	v_pk_fma_f32 v[8:9], v[200:201], v[26:27], v[208:209]
	v_pk_mul_f32 v[12:13], v[28:29], v[24:25] op_sel_hi:[1,0]
	s_nop 0
	v_pk_fma_f32 v[10:11], v[202:203], v[12:13], v[210:211]
	v_pk_mul_f32 v[12:13], v[30:31], v[24:25] op_sel_hi:[1,0]
	s_nop 0
	v_pk_fma_f32 v[4:5], v[204:205], v[12:13], v[212:213]
	v_pk_mul_f32 v[0:1], v[32:33], v[24:25] op_sel_hi:[1,0]
	s_nop 0
	v_pk_fma_f32 v[6:7], v[0:1], v[206:207], v[214:215]
	v_cvt_pk_bf16_f32 v2, v4, v5
	v_add_co_u32_e32 v4, vcc, s10, v90
	v_cvt_pk_bf16_f32 v0, v8, v9
	v_cvt_pk_bf16_f32 v1, v10, v11
	v_cvt_pk_bf16_f32 v3, v6, v7
	v_addc_co_u32_e32 v5, vcc, -1, v91, vcc
	global_store_dwordx4 v[4:5], v[0:3], off
	s_movk_i32 s10, 0x3fff
	v_pk_fma_f32 v[4:5], v[16:17], v[216:217], v[224:225]
	v_pk_mul_f32 v[12:13], v[18:19], v[24:25] op_sel_hi:[1,0]
	s_nop 0
	v_pk_fma_f32 v[6:7], v[12:13], v[218:219], v[226:227]
	v_pk_mul_f32 v[12:13], v[20:21], v[24:25] op_sel_hi:[1,0]
	s_nop 0
	v_pk_fma_f32 v[8:9], v[12:13], v[220:221], v[228:229]
	v_pk_mul_f32 v[0:1], v[22:23], v[24:25] op_sel_hi:[1,0]
	s_nop 0
	v_pk_fma_f32 v[10:11], v[0:1], v[222:223], v[230:231]
	v_cvt_pk_bf16_f32 v0, v4, v5
	v_add_co_u32_e32 v4, vcc, 0xf2b01000, v90
	v_cvt_pk_bf16_f32 v1, v6, v7
	s_nop 0
	v_addc_co_u32_e32 v5, vcc, -1, v91, vcc
	v_cmp_lt_i32_e32 vcc, s10, v80
	v_cvt_pk_bf16_f32 v2, v8, v9
	v_cvt_pk_bf16_f32 v3, v10, v11
	v_lshl_add_u64 v[90:91], v[90:91], 0, s[4:5]
	s_or_b64 s[6:7], vcc, s[6:7]
	global_store_dwordx4 v[4:5], v[0:3], off offset:-3072
	s_andn2_b64 exec, exec, s[6:7]
	s_cbranch_execz .LBB0_1014
.LBB0_1012:
	s_waitcnt vmcnt(2)
	v_mov_b32_e32 v24, 0
	v_mov_b32_e32 v25, 0
	s_and_saveexec_b64 s[10:11], s[0:1]
	s_cbranch_execz .LBB0_1011
	v_lshl_add_u32 v0, v244, 2, 0
	v_add_u32_e32 v0, 0x1ec10, v0
	ds_read_b32 v0, v0
	v_mov_b32_e32 v24, v246
	s_waitcnt lgkmcnt(0)
	v_add_u32_e32 v25, v245, v0
	s_branch .LBB0_1011

.LBB0_2549:
	s_or_b64 exec, exec, s[0:1]
	s_waitcnt lgkmcnt(0)
	s_barrier
	s_getreg_b32 s0, hwreg(HW_REG_HW_ID, 0, 6)
	s_lshl_b32 s0, s0, 2
	s_add_i32 s0, s0, 0x27000
	v_mov_b32_e32 v0, s0
	ds_read_b32 v0, v0
	v_mov_b32_e32 v1, 0
	v_mov_b32_e32 v4, 0
	s_waitcnt lgkmcnt(0)
	v_readfirstlane_b32 s0, v0
	v_mbcnt_lo_u32_b32 v0, -1, v1
	v_mbcnt_hi_u32_b32 v0, -1, v0
	v_lshl_or_b32 v2, s0, 6, v0
	s_getreg_b32 s0, hwreg(HW_REG_HW_ID, 0, 6)
	s_lshl_b32 s0, s0, 2
	s_add_i32 s0, s0, 0x27000
	v_mov_b32_e32 v0, s0
	ds_read_b32 v0, v0
	v_mov_b32_e32 v1, 0
	s_waitcnt lgkmcnt(0)
	v_readfirstlane_b32 s0, v0
	v_mbcnt_lo_u32_b32 v0, -1, v1
	v_mbcnt_hi_u32_b32 v0, -1, v0
	v_lshl_or_b32 v3, s0, 6, v0
	s_getreg_b32 s0, hwreg(HW_REG_HW_ID, 0, 6)
	s_lshl_b32 s0, s0, 2
	s_add_i32 s0, s0, 0x27000
	v_mov_b32_e32 v0, s0
	ds_read_b32 v0, v0
	v_mov_b32_e32 v1, 0
	s_waitcnt lgkmcnt(0)
	v_readfirstlane_b32 s0, v0
	v_mbcnt_lo_u32_b32 v0, -1, v4
	v_mbcnt_hi_u32_b32 v0, -1, v0
	v_lshl_or_b32 v0, s0, 6, v0
	s_movk_i32 s0, 0x100
	s_nop 0
	v_cmp_gt_i32_e32 vcc, s0, v0
	v_lshl_add_u32 v4, v0, 2, 0
	v_ashrrev_i32_e32 v0, 6, v3
	v_readlane_b32 s0, v253, 30
	s_waitcnt lgkmcnt(0)
	s_barrier
	v_add_u32_e32 v24, s0, v0
	s_movk_i32 s0, 0x4000
	v_cmp_gt_i32_e32 vcc, s0, v24
	s_and_saveexec_b64 s[0:1], vcc
	s_cbranch_execz .LBB0_2595
	v_readlane_b32 s0, v253, 4
	v_readlane_b32 s2, v253, 6
	v_readlane_b32 s14, v253, 18
	v_readlane_b32 s3, v253, 7
	v_readlane_b32 s15, v253, 19
	s_add_u32 s2, s14, 0x1000
	v_and_b32_e32 v1, 63, v2
	v_readlane_b32 s6, v253, 10
	s_addc_u32 s3, s15, 0
	v_lshlrev_b32_e32 v2, 5, v1
	v_mov_b32_e32 v3, 0
	v_readlane_b32 s7, v253, 11
	s_add_u32 s6, s64, 0x1000
	v_or_b32_e32 v4, 0x800, v2
	v_mov_b32_e32 v5, v3
	s_addc_u32 s7, s65, 0
	v_lshl_add_u64 v[26:27], s[2:3], 0, v[2:3]
	v_lshl_add_u64 v[30:31], s[2:3], 0, v[4:5]
	v_readlane_b32 s2, v254, 3
	v_readlane_b32 s12, v253, 16
	v_readlane_b32 s13, v253, 17
	s_cmp_lg_u64 s[66:67], 0
	v_lshl_add_u64 v[32:33], s[6:7], 0, v[4:5]
	v_lshlrev_b32_e32 v4, 4, v1
	v_readlane_b32 s3, v254, 4
	v_readlane_b32 s1, v253, 5
	s_cselect_b64 s[12:13], -1, 0
	v_lshl_add_u64 v[34:35], s[2:3], 0, v[4:5]
	s_lshl_b32 s2, s72, 6
	v_lshlrev_b32_e32 v0, 3, v0
	v_ashrrev_i32_e32 v25, 31, v24
	v_cmp_gt_u32_e64 s[0:1], 8, v1
	v_add3_u32 v36, s2, v0, v1
	v_readlane_b32 s2, v253, 2
	v_lshlrev_b64 v[0:1], 11, v[24:25]
	v_readlane_b32 s11, v253, 15
	v_readlane_b32 s3, v253, 3
	v_or_b32_e32 v0, v0, v4
	s_lshl_b32 s11, s2, 6
	v_lshl_add_u64 v[0:1], s[70:71], 0, v[0:1]
	s_mov_b64 s[2:3], 0xd60d900
	v_lshl_add_u64 v[38:39], v[0:1], 0, s[2:3]
	v_lshlrev_b64 v[0:1], 12, v[24:25]
	v_or_b32_e32 v0, v0, v2
	v_lshl_add_u64 v[0:1], s[66:67], 0, v[0:1]
	s_mov_b64 s[2:3], 0x800
	v_readlane_b32 s4, v253, 8
	v_readlane_b32 s5, v253, 9
	v_readlane_b32 s8, v253, 12
	v_readlane_b32 s9, v253, 13
	v_readlane_b32 s10, v253, 14
	s_ashr_i32 s75, s74, 31
	v_lshl_add_u64 v[40:41], v[0:1], 0, s[2:3]
	v_cndmask_b32_e64 v0, 0, 1, s[12:13]
	s_mov_b64 s[4:5], 0
	v_lshl_add_u64 v[28:29], s[6:7], 0, v[2:3]
	s_lshl_b64 s[6:7], s[74:75], 11
	s_lshl_b64 s[8:9], s[74:75], 12
	s_mov_b32 s10, 0x3fb504f3
	v_mov_b32_e32 v25, 0x3727c5ac
	s_mov_b32 s15, 0x800000
	s_movk_i32 s17, 0x3fff
	v_cmp_ne_u32_e64 s[2:3], 1, v0
	v_min_u32_e32 v240, 0x1ffff, v36
	v_mov_b32_e32 v241, 0
	v_readlane_b32 s98, v253, 55
	v_readlane_b32 s99, v253, 56
	v_lshlrev_b64 v[240:241], 2, v[240:241]
	s_nop 1
	v_lshl_add_u64 v[242:243], s[98:99], 0, v[240:241]
	global_load_dword v244, v[242:243], off
	v_readlane_b32 s98, v253, 59
	v_readlane_b32 s99, v253, 60
	s_nop 1
	v_lshl_add_u64 v[242:243], s[98:99], 0, v[240:241]
	global_load_dword v245, v[242:243], off
	v_readlane_b32 s98, v253, 57
	v_readlane_b32 s99, v253, 58
	s_nop 1
	v_lshl_add_u64 v[242:243], s[98:99], 0, v[240:241]
	global_load_dword v246, v[242:243], off
	global_load_dwordx4 v[200:203], v[26:27], off
	global_load_dwordx4 v[204:207], v[28:29], off
	global_load_dwordx4 v[208:211], v[26:27], off offset:16
	global_load_dwordx4 v[212:215], v[28:29], off offset:16
	global_load_dwordx4 v[216:219], v[30:31], off
	global_load_dwordx4 v[220:223], v[32:33], off
	global_load_dwordx4 v[224:227], v[30:31], off offset:16
	global_load_dwordx4 v[228:231], v[32:33], off offset:16
	s_waitcnt vmcnt(0)
	s_branch .LBB0_2591
.Lopt20_cb1_skip:
	s_waitcnt vmcnt(0)
.LBB0_2590:
	v_add_u32_e32 v24, s74, v24
	v_cmp_lt_i32_e32 vcc, s17, v24
	v_add_u32_e32 v36, s11, v36
	v_lshl_add_u64 v[38:39], v[38:39], 0, s[6:7]
	s_or_b64 s[4:5], vcc, s[4:5]
	v_lshl_add_u64 v[40:41], v[40:41], 0, s[8:9]
	s_andn2_b64 exec, exec, s[4:5]
	s_cbranch_execz .LBB0_2595
.LBB0_2591:
	v_mov_b32_e32 v0, 0
	v_mov_b32_e32 v1, 0
	s_and_saveexec_b64 s[12:13], s[0:1]
	s_cbranch_execz .LBB0_2593
	s_waitcnt vmcnt(4)
	v_lshl_add_u32 v2, v244, 2, 0
	v_add_u32_e32 v2, 0x1ec10, v2
	ds_read_b32 v2, v2
	v_mov_b32_e32 v0, v246
	s_waitcnt lgkmcnt(0)
	v_add_u32_e32 v1, v245, v2
.LBB0_2593:
	s_or_b64 exec, exec, s[12:13]
	v_readlane_b32 s12, v1, 0
	s_ashr_i32 s13, s12, 31
	s_lshl_b64 s[12:13], s[12:13], 11
	v_lshl_add_u64 v[98:99], v[34:35], 0, s[12:13]
	v_readlane_b32 s12, v1, 1
	s_ashr_i32 s13, s12, 31
	s_lshl_b64 s[12:13], s[12:13], 11
	v_lshl_add_u64 v[100:101], v[34:35], 0, s[12:13]
	v_readlane_b32 s12, v1, 2
	s_ashr_i32 s13, s12, 31
	s_lshl_b64 s[12:13], s[12:13], 11
	v_add_u32_e32 v2, 0x20000, v24
	v_lshl_add_u64 v[102:103], v[34:35], 0, s[12:13]
	v_readlane_b32 s12, v1, 3
	v_ashrrev_i32_e32 v3, 31, v2
	s_ashr_i32 s13, s12, 31
	v_lshlrev_b64 v[2:3], 11, v[2:3]
	s_lshl_b64 s[12:13], s[12:13], 11
	v_lshl_add_u64 v[2:3], v[34:35], 0, v[2:3]
	v_lshl_add_u64 v[104:105], v[34:35], 0, s[12:13]
	v_readlane_b32 s12, v1, 4
	global_load_dwordx4 v[42:45], v[38:39], off offset:-1024
	global_load_dwordx4 v[46:49], v[2:3], off
	s_ashr_i32 s13, s12, 31
	global_load_dwordx4 v[50:53], v[98:99], off
	global_load_dwordx4 v[54:57], v[100:101], off
	s_lshl_b64 s[12:13], s[12:13], 11
	global_load_dwordx4 v[58:61], v[102:103], off
	global_load_dwordx4 v[62:65], v[104:105], off
	v_lshl_add_u64 v[106:107], v[34:35], 0, s[12:13]
	global_load_dwordx4 v[66:69], v[106:107], off
	global_load_dwordx4 v[70:73], v[38:39], off
	global_load_dwordx4 v[74:77], v[2:3], off offset:1024
	v_readlane_b32 s28, v1, 5
	v_readlane_b32 s30, v1, 6
	v_readlane_b32 s34, v1, 7
	s_ashr_i32 s29, s28, 31
	s_ashr_i32 s31, s30, 31
	s_ashr_i32 s35, s34, 31
	s_lshl_b64 s[28:29], s[28:29], 11
	s_lshl_b64 s[30:31], s[30:31], 11
	s_lshl_b64 s[34:35], s[34:35], 11
	v_readlane_b32 s26, v0, 0
	v_readlane_b32 s22, v0, 1
	v_readlane_b32 s20, v0, 2
	v_readlane_b32 s16, v0, 3
	v_readlane_b32 s14, v0, 4
	v_readlane_b32 s12, v0, 5
	v_readlane_b32 s18, v0, 6
	v_readlane_b32 s24, v0, 7
	v_lshl_add_u64 v[108:109], v[34:35], 0, s[28:29]
	v_lshl_add_u64 v[110:111], v[34:35], 0, s[30:31]
	v_lshl_add_u64 v[112:113], v[34:35], 0, s[34:35]
	global_load_dwordx4 v[78:81], v[98:99], off offset:1024
	global_load_dwordx4 v[82:85], v[100:101], off offset:1024
	global_load_dwordx4 v[86:89], v[102:103], off offset:1024
	global_load_dwordx4 v[90:93], v[104:105], off offset:1024
	global_load_dwordx4 v[94:97], v[106:107], off offset:1024
	global_load_dwordx4 v[20:23], v[108:109], off
	global_load_dwordx4 v[8:11], v[108:109], off offset:1024
	global_load_dwordx4 v[16:19], v[110:111], off
	global_load_dwordx4 v[4:7], v[110:111], off offset:1024
	global_load_dwordx4 v[12:15], v[112:113], off
	global_load_dwordx4 v[0:3], v[112:113], off offset:1024
	v_add_u32_e32 v240, s11, v36
	v_min_u32_e32 v240, 0x1ffff, v240
	v_mov_b32_e32 v241, 0
	v_readlane_b32 s98, v253, 55
	v_readlane_b32 s99, v253, 56
	v_lshlrev_b64 v[240:241], 2, v[240:241]
	s_nop 1
	v_lshl_add_u64 v[242:243], s[98:99], 0, v[240:241]
	global_load_dword v244, v[242:243], off
	v_readlane_b32 s98, v253, 59
	v_readlane_b32 s99, v253, 60
	s_nop 1
	v_lshl_add_u64 v[242:243], s[98:99], 0, v[240:241]
	global_load_dword v245, v[242:243], off
	v_readlane_b32 s98, v253, 57
	v_readlane_b32 s99, v253, 58
	s_nop 1
	v_lshl_add_u64 v[242:243], s[98:99], 0, v[240:241]
	global_load_dword v246, v[242:243], off
	s_and_b64 vcc, exec, s[2:3]
	s_waitcnt vmcnt(22)
	v_lshlrev_b32_e32 v98, 16, v42
	v_and_b32_e32 v99, 0xffff0000, v42
	v_lshlrev_b32_e32 v42, 16, v43
	v_and_b32_e32 v43, 0xffff0000, v43
	s_waitcnt vmcnt(21)
	v_lshlrev_b32_e32 v100, 16, v46
	v_and_b32_e32 v101, 0xffff0000, v46
	v_lshlrev_b32_e32 v46, 16, v47
	v_and_b32_e32 v47, 0xffff0000, v47
	s_waitcnt vmcnt(20)
	v_lshlrev_b32_e32 v102, 16, v50
	v_and_b32_e32 v103, 0xffff0000, v50
	v_lshlrev_b32_e32 v50, 16, v51
	v_and_b32_e32 v51, 0xffff0000, v51
	v_pk_fma_f32 v[98:99], v[98:99], s[10:11], v[100:101] op_sel_hi:[1,0,1]
	v_pk_fma_f32 v[42:43], v[42:43], s[10:11], v[46:47] op_sel_hi:[1,0,1]
	s_waitcnt vmcnt(19)
	v_lshlrev_b32_e32 v104, 16, v54
	v_and_b32_e32 v105, 0xffff0000, v54
	s_waitcnt vmcnt(18)
	v_lshlrev_b32_e32 v106, 16, v58
	v_and_b32_e32 v107, 0xffff0000, v58
	s_waitcnt vmcnt(17)
	v_lshlrev_b32_e32 v108, 16, v62
	v_and_b32_e32 v109, 0xffff0000, v62
	s_waitcnt vmcnt(16)
	v_lshlrev_b32_e32 v110, 16, v66
	v_and_b32_e32 v111, 0xffff0000, v66
	v_pk_fma_f32 v[46:47], s[26:27], v[102:103], v[98:99] op_sel_hi:[0,1,1]
	v_pk_fma_f32 v[42:43], s[26:27], v[50:51], v[42:43] op_sel_hi:[0,1,1]
	v_lshlrev_b32_e32 v50, 16, v55
	v_and_b32_e32 v51, 0xffff0000, v55
	v_lshlrev_b32_e32 v54, 16, v59
	v_and_b32_e32 v55, 0xffff0000, v59
	v_lshlrev_b32_e32 v58, 16, v63
	v_and_b32_e32 v59, 0xffff0000, v63
	v_lshlrev_b32_e32 v62, 16, v67
	v_and_b32_e32 v63, 0xffff0000, v67
	v_lshlrev_b32_e32 v66, 16, v44
	v_and_b32_e32 v67, 0xffff0000, v44
	v_lshlrev_b32_e32 v98, 16, v48
	v_and_b32_e32 v99, 0xffff0000, v48
	v_lshlrev_b32_e32 v44, 16, v45
	v_and_b32_e32 v45, 0xffff0000, v45
	v_lshlrev_b32_e32 v48, 16, v49
	v_and_b32_e32 v49, 0xffff0000, v49
	v_pk_fma_f32 v[66:67], v[66:67], s[10:11], v[98:99] op_sel_hi:[1,0,1]
	v_lshlrev_b32_e32 v98, 16, v52
	v_and_b32_e32 v99, 0xffff0000, v52
	v_pk_fma_f32 v[44:45], v[44:45], s[10:11], v[48:49] op_sel_hi:[1,0,1]
	v_lshlrev_b32_e32 v48, 16, v53
	v_and_b32_e32 v49, 0xffff0000, v53
	v_pk_fma_f32 v[66:67], s[26:27], v[98:99], v[66:67] op_sel_hi:[0,1,1]
	v_lshlrev_b32_e32 v98, 16, v56
	v_and_b32_e32 v99, 0xffff0000, v56
	v_lshlrev_b32_e32 v100, 16, v60
	v_and_b32_e32 v101, 0xffff0000, v60
	v_lshlrev_b32_e32 v102, 16, v64
	v_and_b32_e32 v103, 0xffff0000, v64
	v_lshlrev_b32_e32 v112, 16, v68
	v_and_b32_e32 v113, 0xffff0000, v68
	v_pk_fma_f32 v[44:45], s[26:27], v[48:49], v[44:45] op_sel_hi:[0,1,1]
	v_lshlrev_b32_e32 v48, 16, v57
	v_and_b32_e32 v49, 0xffff0000, v57
	v_lshlrev_b32_e32 v52, 16, v61
	v_and_b32_e32 v53, 0xffff0000, v61
	v_lshlrev_b32_e32 v56, 16, v65
	v_and_b32_e32 v57, 0xffff0000, v65
	v_lshlrev_b32_e32 v60, 16, v69
	v_and_b32_e32 v61, 0xffff0000, v69
	s_waitcnt vmcnt(15)
	v_lshlrev_b32_e32 v64, 16, v70
	v_and_b32_e32 v65, 0xffff0000, v70
	s_waitcnt vmcnt(14)
	v_lshlrev_b32_e32 v68, 16, v74
	v_and_b32_e32 v69, 0xffff0000, v74
	v_lshlrev_b32_e32 v70, 16, v71
	v_and_b32_e32 v71, 0xffff0000, v71
	v_lshlrev_b32_e32 v74, 16, v75
	v_and_b32_e32 v75, 0xffff0000, v75
	v_pk_fma_f32 v[64:65], v[64:65], s[10:11], v[68:69] op_sel_hi:[1,0,1]
	s_waitcnt vmcnt(13)
	v_lshlrev_b32_e32 v68, 16, v78
	v_and_b32_e32 v69, 0xffff0000, v78
	v_pk_fma_f32 v[70:71], v[70:71], s[10:11], v[74:75] op_sel_hi:[1,0,1]
	v_lshlrev_b32_e32 v74, 16, v79
	v_and_b32_e32 v75, 0xffff0000, v79
	v_pk_fma_f32 v[46:47], s[22:23], v[104:105], v[46:47] op_sel_hi:[0,1,1]
	v_pk_fma_f32 v[64:65], s[26:27], v[68:69], v[64:65] op_sel_hi:[0,1,1]
	s_waitcnt vmcnt(12)
	v_lshlrev_b32_e32 v68, 16, v82
	v_and_b32_e32 v69, 0xffff0000, v82
	s_waitcnt vmcnt(11)
	v_lshlrev_b32_e32 v114, 16, v86
	v_and_b32_e32 v115, 0xffff0000, v86
	s_waitcnt vmcnt(10)
	v_lshlrev_b32_e32 v116, 16, v90
	v_and_b32_e32 v117, 0xffff0000, v90
	s_waitcnt vmcnt(9)
	v_lshlrev_b32_e32 v118, 16, v94
	v_and_b32_e32 v119, 0xffff0000, v94
	v_pk_fma_f32 v[70:71], s[26:27], v[74:75], v[70:71] op_sel_hi:[0,1,1]
	v_lshlrev_b32_e32 v74, 16, v83
	v_and_b32_e32 v75, 0xffff0000, v83
	v_lshlrev_b32_e32 v78, 16, v87
	v_and_b32_e32 v79, 0xffff0000, v87
	v_lshlrev_b32_e32 v82, 16, v91
	v_and_b32_e32 v83, 0xffff0000, v91
	v_lshlrev_b32_e32 v86, 16, v95
	v_and_b32_e32 v87, 0xffff0000, v95
	v_lshlrev_b32_e32 v90, 16, v72
	v_and_b32_e32 v91, 0xffff0000, v72
	v_lshlrev_b32_e32 v94, 16, v76
	v_and_b32_e32 v95, 0xffff0000, v76
	v_lshlrev_b32_e32 v72, 16, v73
	v_and_b32_e32 v73, 0xffff0000, v73
	v_lshlrev_b32_e32 v76, 16, v77
	v_and_b32_e32 v77, 0xffff0000, v77
	v_pk_fma_f32 v[46:47], s[20:21], v[106:107], v[46:47] op_sel_hi:[0,1,1]
	v_pk_fma_f32 v[90:91], v[90:91], s[10:11], v[94:95] op_sel_hi:[1,0,1]
	v_lshlrev_b32_e32 v94, 16, v80
	v_and_b32_e32 v95, 0xffff0000, v80
	v_pk_fma_f32 v[72:73], v[72:73], s[10:11], v[76:77] op_sel_hi:[1,0,1]
	v_lshlrev_b32_e32 v76, 16, v81
	v_and_b32_e32 v77, 0xffff0000, v81
	v_pk_fma_f32 v[46:47], s[16:17], v[108:109], v[46:47] op_sel_hi:[0,1,1]
	v_pk_fma_f32 v[90:91], s[26:27], v[94:95], v[90:91] op_sel_hi:[0,1,1]
	v_lshlrev_b32_e32 v94, 16, v84
	v_and_b32_e32 v95, 0xffff0000, v84
	v_lshlrev_b32_e32 v122, 16, v92
	v_and_b32_e32 v123, 0xffff0000, v92
	v_pk_fma_f32 v[72:73], s[26:27], v[76:77], v[72:73] op_sel_hi:[0,1,1]
	v_lshlrev_b32_e32 v76, 16, v85
	v_and_b32_e32 v77, 0xffff0000, v85
	v_lshlrev_b32_e32 v84, 16, v93
	v_and_b32_e32 v85, 0xffff0000, v93
	v_pk_fma_f32 v[46:47], s[14:15], v[110:111], v[46:47] op_sel_hi:[0,1,1]
	s_waitcnt vmcnt(8)
	v_lshlrev_b32_e32 v92, 16, v20
	v_and_b32_e32 v93, 0xffff0000, v20
	v_pk_fma_f32 v[42:43], s[22:23], v[50:51], v[42:43] op_sel_hi:[0,1,1]
	v_pk_fma_f32 v[46:47], s[12:13], v[92:93], v[46:47] op_sel_hi:[0,1,1]
	s_waitcnt vmcnt(6)
	v_lshlrev_b32_e32 v92, 16, v16
	v_and_b32_e32 v93, 0xffff0000, v16
	v_pk_fma_f32 v[42:43], s[20:21], v[54:55], v[42:43] op_sel_hi:[0,1,1]
	v_pk_fma_f32 v[46:47], s[18:19], v[92:93], v[46:47] op_sel_hi:[0,1,1]
	s_waitcnt vmcnt(4)
	v_lshlrev_b32_e32 v92, 16, v12
	v_and_b32_e32 v93, 0xffff0000, v12
	v_pk_fma_f32 v[42:43], s[16:17], v[58:59], v[42:43] op_sel_hi:[0,1,1]
	v_pk_fma_f32 v[46:47], s[24:25], v[92:93], v[46:47] op_sel_hi:[0,1,1]
	v_pk_fma_f32 v[42:43], s[14:15], v[62:63], v[42:43] op_sel_hi:[0,1,1]
	v_lshlrev_b32_e32 v20, 16, v21
	v_and_b32_e32 v21, 0xffff0000, v21
	v_add_f32_e32 v12, 0, v46
	v_pk_fma_f32 v[20:21], s[12:13], v[20:21], v[42:43] op_sel_hi:[0,1,1]
	v_lshlrev_b32_e32 v16, 16, v17
	v_and_b32_e32 v17, 0xffff0000, v17
	v_add_f32_e32 v37, v47, v12
	v_pk_fma_f32 v[16:17], s[18:19], v[16:17], v[20:21] op_sel_hi:[0,1,1]
	v_lshlrev_b32_e32 v12, 16, v13
	v_and_b32_e32 v13, 0xffff0000, v13
	v_pk_fma_f32 v[16:17], s[24:25], v[12:13], v[16:17] op_sel_hi:[0,1,1]
	v_add_f32_e32 v12, v16, v37
	v_add_f32_e32 v37, v17, v12
	v_pk_fma_f32 v[12:13], s[22:23], v[98:99], v[66:67] op_sel_hi:[0,1,1]
	v_pk_fma_f32 v[12:13], s[20:21], v[100:101], v[12:13] op_sel_hi:[0,1,1]
	v_pk_fma_f32 v[12:13], s[16:17], v[102:103], v[12:13] op_sel_hi:[0,1,1]
	v_pk_fma_f32 v[12:13], s[14:15], v[112:113], v[12:13] op_sel_hi:[0,1,1]
	v_lshlrev_b32_e32 v20, 16, v22
	v_and_b32_e32 v21, 0xffff0000, v22
	v_pk_fma_f32 v[12:13], s[12:13], v[20:21], v[12:13] op_sel_hi:[0,1,1]
	v_lshlrev_b32_e32 v20, 16, v18
	v_and_b32_e32 v21, 0xffff0000, v18
	v_pk_fma_f32 v[12:13], s[18:19], v[20:21], v[12:13] op_sel_hi:[0,1,1]
	v_lshlrev_b32_e32 v20, 16, v14
	v_and_b32_e32 v21, 0xffff0000, v14
	v_pk_fma_f32 v[20:21], s[24:25], v[20:21], v[12:13] op_sel_hi:[0,1,1]
	v_add_f32_e32 v12, v20, v37
	v_add_f32_e32 v37, v21, v12
	v_pk_fma_f32 v[12:13], s[22:23], v[48:49], v[44:45] op_sel_hi:[0,1,1]
	v_pk_fma_f32 v[12:13], s[20:21], v[52:53], v[12:13] op_sel_hi:[0,1,1]
	v_pk_fma_f32 v[12:13], s[16:17], v[56:57], v[12:13] op_sel_hi:[0,1,1]
	v_pk_fma_f32 v[12:13], s[14:15], v[60:61], v[12:13] op_sel_hi:[0,1,1]
	v_lshlrev_b32_e32 v22, 16, v23
	v_and_b32_e32 v23, 0xffff0000, v23
	v_pk_fma_f32 v[12:13], s[12:13], v[22:23], v[12:13] op_sel_hi:[0,1,1]
	v_lshlrev_b32_e32 v18, 16, v19
	v_and_b32_e32 v19, 0xffff0000, v19
	v_pk_fma_f32 v[12:13], s[18:19], v[18:19], v[12:13] op_sel_hi:[0,1,1]
	v_lshlrev_b32_e32 v14, 16, v15
	v_and_b32_e32 v15, 0xffff0000, v15
	v_pk_fma_f32 v[18:19], s[24:25], v[14:15], v[12:13] op_sel_hi:[0,1,1]
	v_add_f32_e32 v12, v18, v37
	v_add_f32_e32 v37, v19, v12
	v_pk_fma_f32 v[12:13], s[22:23], v[68:69], v[64:65] op_sel_hi:[0,1,1]
	v_pk_fma_f32 v[12:13], s[20:21], v[114:115], v[12:13] op_sel_hi:[0,1,1]
	v_pk_fma_f32 v[12:13], s[16:17], v[116:117], v[12:13] op_sel_hi:[0,1,1]
	v_pk_fma_f32 v[12:13], s[14:15], v[118:119], v[12:13] op_sel_hi:[0,1,1]
	v_lshlrev_b32_e32 v14, 16, v8
	v_and_b32_e32 v15, 0xffff0000, v8
	v_pk_fma_f32 v[12:13], s[12:13], v[14:15], v[12:13] op_sel_hi:[0,1,1]
	v_lshlrev_b32_e32 v14, 16, v4
	v_and_b32_e32 v15, 0xffff0000, v4
	v_pk_fma_f32 v[12:13], s[18:19], v[14:15], v[12:13] op_sel_hi:[0,1,1]
	s_waitcnt vmcnt(3)
	v_lshlrev_b32_e32 v14, 16, v0
	v_and_b32_e32 v15, 0xffff0000, v0
	v_pk_fma_f32 v[22:23], s[24:25], v[14:15], v[12:13] op_sel_hi:[0,1,1]
	v_pk_fma_f32 v[12:13], s[22:23], v[74:75], v[70:71] op_sel_hi:[0,1,1]
	v_pk_fma_f32 v[12:13], s[20:21], v[78:79], v[12:13] op_sel_hi:[0,1,1]
	v_pk_fma_f32 v[12:13], s[16:17], v[82:83], v[12:13] op_sel_hi:[0,1,1]
	v_pk_fma_f32 v[12:13], s[14:15], v[86:87], v[12:13] op_sel_hi:[0,1,1]
	v_lshlrev_b32_e32 v8, 16, v9
	v_and_b32_e32 v9, 0xffff0000, v9
	v_add_f32_e32 v0, v22, v37
	v_pk_fma_f32 v[8:9], s[12:13], v[8:9], v[12:13] op_sel_hi:[0,1,1]
	v_lshlrev_b32_e32 v4, 16, v5
	v_and_b32_e32 v5, 0xffff0000, v5
	v_add_f32_e32 v14, v23, v0
	v_pk_fma_f32 v[4:5], s[18:19], v[4:5], v[8:9] op_sel_hi:[0,1,1]
	v_lshlrev_b32_e32 v0, 16, v1
	v_and_b32_e32 v1, 0xffff0000, v1
	v_pk_fma_f32 v[0:1], s[24:25], v[0:1], v[4:5] op_sel_hi:[0,1,1]
	v_add_f32_e32 v4, v0, v14
	v_lshlrev_b32_e32 v120, 16, v88
	v_and_b32_e32 v121, 0xffff0000, v88
	v_add_f32_e32 v12, v1, v4
	v_pk_fma_f32 v[4:5], s[22:23], v[94:95], v[90:91] op_sel_hi:[0,1,1]
	v_pk_fma_f32 v[4:5], s[20:21], v[120:121], v[4:5] op_sel_hi:[0,1,1]
	v_lshlrev_b32_e32 v124, 16, v96
	v_and_b32_e32 v125, 0xffff0000, v96
	v_pk_fma_f32 v[4:5], s[16:17], v[122:123], v[4:5] op_sel_hi:[0,1,1]
	v_pk_fma_f32 v[4:5], s[14:15], v[124:125], v[4:5] op_sel_hi:[0,1,1]
	v_lshlrev_b32_e32 v8, 16, v10
	v_and_b32_e32 v9, 0xffff0000, v10
	v_pk_fma_f32 v[4:5], s[12:13], v[8:9], v[4:5] op_sel_hi:[0,1,1]
	v_lshlrev_b32_e32 v8, 16, v6
	v_and_b32_e32 v9, 0xffff0000, v6
	v_pk_fma_f32 v[4:5], s[18:19], v[8:9], v[4:5] op_sel_hi:[0,1,1]
	v_lshlrev_b32_e32 v8, 16, v2
	v_and_b32_e32 v9, 0xffff0000, v2
	v_lshlrev_b32_e32 v80, 16, v89
	v_and_b32_e32 v81, 0xffff0000, v89
	v_pk_fma_f32 v[42:43], s[24:25], v[8:9], v[4:5] op_sel_hi:[0,1,1]
	v_pk_fma_f32 v[4:5], s[22:23], v[76:77], v[72:73] op_sel_hi:[0,1,1]
	v_pk_fma_f32 v[4:5], s[20:21], v[80:81], v[4:5] op_sel_hi:[0,1,1]
	v_lshlrev_b32_e32 v88, 16, v97
	v_and_b32_e32 v89, 0xffff0000, v97
	v_pk_fma_f32 v[4:5], s[16:17], v[84:85], v[4:5] op_sel_hi:[0,1,1]
	v_pk_fma_f32 v[4:5], s[14:15], v[88:89], v[4:5] op_sel_hi:[0,1,1]
	v_lshlrev_b32_e32 v8, 16, v11
	v_and_b32_e32 v9, 0xffff0000, v11
	v_add_f32_e32 v2, v42, v12
	v_pk_fma_f32 v[4:5], s[12:13], v[8:9], v[4:5] op_sel_hi:[0,1,1]
	v_lshlrev_b32_e32 v6, 16, v7
	v_and_b32_e32 v7, 0xffff0000, v7
	v_add_f32_e32 v10, v43, v2
	v_pk_fma_f32 v[4:5], s[18:19], v[6:7], v[4:5] op_sel_hi:[0,1,1]
	v_lshlrev_b32_e32 v2, 16, v3
	v_and_b32_e32 v3, 0xffff0000, v3
	v_pk_fma_f32 v[2:3], s[24:25], v[2:3], v[4:5] op_sel_hi:[0,1,1]
	v_add_f32_e32 v4, v2, v10
	v_add_f32_e32 v4, v3, v4
	s_nop 1
	v_add_f32_dpp v4, v4, v4 quad_perm:[1,0,3,2] row_mask:0xf bank_mask:0xf bound_ctrl:1
	s_nop 1
	v_add_f32_dpp v4, v4, v4 quad_perm:[2,3,0,1] row_mask:0xf bank_mask:0xf bound_ctrl:1
	s_nop 1
	v_add_f32_dpp v4, v4, v4 row_half_mirror row_mask:0xf bank_mask:0xf bound_ctrl:1
	s_nop 1
	v_add_f32_dpp v4, v4, v4 row_mirror row_mask:0xf bank_mask:0xf bound_ctrl:1
	v_mov_b32_e32 v5, v4
	s_nop 1
	v_permlane16_swap_b32 v5, v4
	s_nop 0
	v_add_f32_e32 v4, v5, v4
	v_mov_b32_e32 v5, v4
	s_nop 1
	v_permlane32_swap_b32 v4, v5
	s_nop 0
	v_add_f32_e32 v4, v4, v5
	v_mul_f32_e32 v44, 0x3a800000, v4
	v_pk_add_f32 v[12:13], v[46:47], v[44:45] op_sel_hi:[1,0] neg_lo:[0,1] neg_hi:[0,1]
	v_pk_add_f32 v[14:15], v[16:17], v[44:45] op_sel_hi:[1,0] neg_lo:[0,1] neg_hi:[0,1]
	v_pk_mul_f32 v[46:47], v[12:13], v[12:13]
	v_pk_mul_f32 v[16:17], v[14:15], v[14:15]
	v_add_f32_e32 v37, v46, v47
	v_pk_add_f32 v[8:9], v[20:21], v[44:45] op_sel_hi:[1,0] neg_lo:[0,1] neg_hi:[0,1]
	v_add_f32_e32 v16, v16, v37
	v_pk_mul_f32 v[20:21], v[8:9], v[8:9]
	v_add_f32_e32 v16, v17, v16
	v_pk_add_f32 v[10:11], v[18:19], v[44:45] op_sel_hi:[1,0] neg_lo:[0,1] neg_hi:[0,1]
	v_add_f32_e32 v16, v20, v16
	v_pk_mul_f32 v[18:19], v[10:11], v[10:11]
	v_add_f32_e32 v16, v21, v16
	v_pk_add_f32 v[4:5], v[22:23], v[44:45] op_sel_hi:[1,0] neg_lo:[0,1] neg_hi:[0,1]
	v_add_f32_e32 v16, v18, v16
	v_pk_mul_f32 v[22:23], v[4:5], v[4:5]
	v_add_f32_e32 v16, v19, v16
	v_pk_add_f32 v[6:7], v[0:1], v[44:45] op_sel_hi:[1,0] neg_lo:[0,1] neg_hi:[0,1]
	v_add_f32_e32 v16, v22, v16
	v_pk_mul_f32 v[48:49], v[6:7], v[6:7]
	v_add_f32_e32 v16, v23, v16
	v_pk_add_f32 v[0:1], v[42:43], v[44:45] op_sel_hi:[1,0] neg_lo:[0,1] neg_hi:[0,1]
	v_add_f32_e32 v16, v48, v16
	v_pk_mul_f32 v[42:43], v[0:1], v[0:1]
	v_add_f32_e32 v16, v49, v16
	v_pk_add_f32 v[2:3], v[2:3], v[44:45] op_sel_hi:[1,0] neg_lo:[0,1] neg_hi:[0,1]
	v_add_f32_e32 v16, v42, v16
	v_pk_mul_f32 v[44:45], v[2:3], v[2:3]
	v_add_f32_e32 v16, v43, v16
	v_add_f32_e32 v16, v44, v16
	v_add_f32_e32 v16, v45, v16
	s_nop 1
	v_add_f32_dpp v16, v16, v16 quad_perm:[1,0,3,2] row_mask:0xf bank_mask:0xf bound_ctrl:1
	s_nop 1
	v_add_f32_dpp v16, v16, v16 quad_perm:[2,3,0,1] row_mask:0xf bank_mask:0xf bound_ctrl:1
	s_nop 1
	v_add_f32_dpp v16, v16, v16 row_half_mirror row_mask:0xf bank_mask:0xf bound_ctrl:1
	s_nop 1
	v_add_f32_dpp v16, v16, v16 row_mirror row_mask:0xf bank_mask:0xf bound_ctrl:1
	v_mov_b32_e32 v17, v16
	s_nop 1
	v_permlane16_swap_b32 v17, v16
	s_nop 0
	v_add_f32_e32 v16, v17, v16
	v_mov_b32_e32 v17, v16
	s_nop 1
	v_permlane32_swap_b32 v17, v16
	s_cbranch_vccnz .Lopt20_cb1_skip
	v_add_f32_e32 v16, v17, v16
	v_fmamk_f32 v16, v16, 0x3a800000, v25
	v_mul_f32_e32 v17, 0x4b800000, v16
	v_cmp_gt_f32_e32 vcc, s15, v16
	s_nop 1
	v_cndmask_b32_e32 v16, v16, v17, vcc
	v_rsq_f32_e32 v16, v16
	s_nop 0
	v_mul_f32_e32 v17, 0x45800000, v16
	v_cndmask_b32_e32 v22, v16, v17, vcc
	v_pk_mul_f32 v[12:13], v[12:13], v[22:23] op_sel_hi:[1,0]
	v_pk_mul_f32 v[14:15], v[14:15], v[22:23] op_sel_hi:[1,0]
	v_pk_mul_f32 v[8:9], v[8:9], v[22:23] op_sel_hi:[1,0]
	v_pk_mul_f32 v[10:11], v[10:11], v[22:23] op_sel_hi:[1,0]
	v_pk_mul_f32 v[4:5], v[4:5], v[22:23] op_sel_hi:[1,0]
	v_pk_mul_f32 v[6:7], v[6:7], v[22:23] op_sel_hi:[1,0]
	v_pk_mul_f32 v[0:1], v[0:1], v[22:23] op_sel_hi:[1,0]
	v_pk_mul_f32 v[2:3], v[2:3], v[22:23] op_sel_hi:[1,0]
	v_pk_fma_f32 v[12:13], v[12:13], v[200:201], v[204:205]
	v_pk_fma_f32 v[14:15], v[14:15], v[202:203], v[206:207]
	global_store_dwordx4 v[40:41], v[12:15], off offset:-2048
	v_pk_fma_f32 v[8:9], v[8:9], v[208:209], v[212:213]
	v_pk_fma_f32 v[10:11], v[10:11], v[210:211], v[214:215]
	global_store_dwordx4 v[40:41], v[8:11], off offset:-2032
	v_pk_fma_f32 v[4:5], v[4:5], v[216:217], v[220:221]
	v_pk_fma_f32 v[6:7], v[6:7], v[218:219], v[222:223]
	global_store_dwordx4 v[40:41], v[4:7], off
	v_pk_fma_f32 v[0:1], v[0:1], v[224:225], v[228:229]
	v_pk_fma_f32 v[2:3], v[2:3], v[226:227], v[230:231]
	global_store_dwordx4 v[40:41], v[0:3], off offset:16
	s_branch .LBB0_2590
